# DSA indexer score loops: software-pipelined the two heads per iteration (2nd head MFMAs into spare VGPRs), abs folded into v_fma
# speedup vs baseline: 1.0102x; 1.0102x over previous
; __device__ __forceinline__ unsigned ordkey(float f) { const unsigned u = __float_as_uint(f); return u ^ ((unsigned)((int)u >> 31) | 0x80000000u); }
; __device__ __forceinline__ int crow(int r, int hi) { return (r & 3) + 8 * (r >> 2) + 4 * hi; }
; __global__ void __launch_bounds__(NWAVES * 64, 2) mega_fwd(Args args) {
;     ...
;                         for (int h = 0; h < 8; ++h) { fa::f32x16 a;
; #pragma unroll
;                             for (int r = 0; r < 16; ++r) a[r] = 0.f;
;                             a = __builtin_amdgcn_mfma_f32_32x32x16_f16(kf0, __builtin_bit_cast(f16x8, iqL[(2 * h) * 64 + lane]), a, 0, 0, 0);
;                             a = __builtin_amdgcn_mfma_f32_32x32x16_f16(kf1, __builtin_bit_cast(f16x8, iqL[(2 * h + 1) * 64 + lane]), a, 0, 0, 0);
;                             const float sg = ((sgnbits >> h) & 1u) ? -1.f : 1.f;
; #pragma unroll
;                             for (int r = 0; r < 16; ++r) sc[r] = __builtin_fmaf(__builtin_fabsf(a[r]), sg, sc[r]); }
; #pragma unroll
;                         for (int r = 0; r < 16; ++r) keys[ti][16 * half + r] = ordkey(sc[r]);
;                         if (k0 + 63 > 32 * qg) {
; #pragma unroll
;                             for (int r = 0; r < 16; ++r) { const int kidx = k0 + 32 * half + fa::crow(r, hi); keys[ti][16 * half + r] = (kidx <= t) ? keys[ti][16 * half + r] : 0u; } } }
.LBB0_621:
	ds_read_b128 v[18:21], v52
	ds_read_b128 v[114:117], v52 offset:1024
	ds_read_b128 v[224:227], v52 offset:2048
	ds_read_b128 v[176:179], v52 offset:3072
	s_waitcnt lgkmcnt(3)
	v_mfma_f32_32x32x16_f16 v[18:33], v[46:49], v[18:21], 0
	s_waitcnt lgkmcnt(2)
	v_mfma_f32_32x32x16_f16 v[18:33], v[42:45], v[114:117], v[18:33]
	s_waitcnt lgkmcnt(1)
	v_mfma_f32_32x32x16_f16 v[208:223], v[46:49], v[224:227], 0
	s_waitcnt lgkmcnt(0)
	v_mfma_f32_32x32x16_f16 v[208:223], v[42:45], v[176:179], v[208:223]
	v_bfe_u32 v4, v140, s26, 1
	v_cmp_eq_u32_e32 vcc, 0, v4
	v_lshrrev_b32_e32 v180, s26, v140
	v_and_b32_e32 v180, 2, v180
	v_cndmask_b32_e64 v4, -1.0, 1.0, vcc
	v_cmp_eq_u32_e32 vcc, 0, v180
	v_add_u32_e32 v52, 0x1000, v52
	s_add_i32 s26, s26, 2
	v_cndmask_b32_e64 v180, -1.0, 1.0, vcc
	s_cmp_eq_u32 s26, 8
	v_fma_f32 v50, |v20|, v4, v50
	v_fma_f32 v51, |v18|, v4, v51
	v_fma_f32 v114, |v19|, v4, v2
	v_fma_f32 v115, |v21|, v4, v3
	v_fma_f32 v22, |v22|, v4, v6
	v_fma_f32 v23, |v23|, v4, v7
	v_fma_f32 v24, |v24|, v4, v8
	v_fma_f32 v25, |v25|, v4, v9
	v_fma_f32 v26, |v26|, v4, v10
	v_fma_f32 v27, |v27|, v4, v11
	v_fma_f32 v28, |v28|, v4, v12
	v_fma_f32 v29, |v29|, v4, v13
	v_fma_f32 v30, |v30|, v4, v14
	v_fma_f32 v31, |v31|, v4, v15
	v_fma_f32 v32, |v32|, v4, v16
	v_fma_f32 v33, |v33|, v4, v17
	v_fma_f32 v50, |v210|, v180, v50
	v_fma_f32 v51, |v208|, v180, v51
	v_fma_f32 v2, |v209|, v180, v114
	v_fma_f32 v3, |v211|, v180, v115
	v_fma_f32 v8, |v214|, v180, v24
	v_fma_f32 v9, |v215|, v180, v25
	v_fma_f32 v6, |v212|, v180, v22
	v_fma_f32 v7, |v213|, v180, v23
	v_fma_f32 v12, |v218|, v180, v28
	v_fma_f32 v13, |v219|, v180, v29
	v_fma_f32 v10, |v216|, v180, v26
	v_fma_f32 v11, |v217|, v180, v27
	v_fma_f32 v16, |v222|, v180, v32
	v_fma_f32 v17, |v223|, v180, v33
	v_fma_f32 v14, |v220|, v180, v30
	v_fma_f32 v15, |v221|, v180, v31
	s_cbranch_scc0 .LBB0_621
	v_ashrrev_i32_e32 v4, 31, v51
	v_ashrrev_i32_e32 v5, 31, v50
	v_or_b32_e32 v4, 0x80000000, v4
	v_or_b32_e32 v5, 0x80000000, v5
	v_xor_b32_e32 v115, v4, v51
	v_xor_b32_e32 v114, v5, v50
	v_ashrrev_i32_e32 v4, 31, v3
	v_ashrrev_i32_e32 v5, 31, v2
	v_or_b32_e32 v4, 0x80000000, v4
	v_or_b32_e32 v5, 0x80000000, v5
	v_readlane_b32 s26, v254, 33
	v_xor_b32_e32 v117, v4, v3
	v_xor_b32_e32 v116, v5, v2
	v_ashrrev_i32_e32 v2, 31, v6
	v_ashrrev_i32_e32 v3, 31, v7
	v_ashrrev_i32_e32 v4, 31, v8
	v_ashrrev_i32_e32 v5, 31, v9
	s_cmp_gt_u32 s26, s44
	v_bitop3_b32 v53, v5, v9, s68 bitop3:0x36
	v_bitop3_b32 v52, v4, v8, s68 bitop3:0x36
	v_bitop3_b32 v51, v3, v7, s68 bitop3:0x36
	v_bitop3_b32 v50, v2, v6, s68 bitop3:0x36
	v_ashrrev_i32_e32 v2, 31, v10
	v_ashrrev_i32_e32 v3, 31, v11
	v_ashrrev_i32_e32 v4, 31, v12
	v_ashrrev_i32_e32 v5, 31, v13
	s_cselect_b64 s[40:41], -1, 0
	v_bitop3_b32 v45, v5, v13, s68 bitop3:0x36
	v_bitop3_b32 v44, v4, v12, s68 bitop3:0x36
	v_bitop3_b32 v43, v3, v11, s68 bitop3:0x36
	v_bitop3_b32 v42, v2, v10, s68 bitop3:0x36
	v_ashrrev_i32_e32 v2, 31, v14
	v_ashrrev_i32_e32 v3, 31, v15
	v_ashrrev_i32_e32 v4, 31, v16
	v_ashrrev_i32_e32 v5, 31, v17
	v_add_u32_e32 v118, s18, v142
	v_bitop3_b32 v49, v5, v17, s68 bitop3:0x36
	v_bitop3_b32 v48, v4, v16, s68 bitop3:0x36
	v_bitop3_b32 v47, v3, v15, s68 bitop3:0x36
	v_bitop3_b32 v46, v2, v14, s68 bitop3:0x36
	s_and_b64 vcc, exec, s[40:41]
	s_cbranch_vccz .LBB0_624
	v_or_b32_e32 v2, 2, v118
	v_cmp_le_i32_e32 vcc, v118, v124
	v_add_u32_e32 v5, 11, v118
	v_add_u32_e32 v4, 10, v118
	v_cndmask_b32_e32 v115, 0, v115, vcc
	v_cmp_le_i32_e32 vcc, v2, v124
	v_or_b32_e32 v2, 3, v118
	v_add_u32_e32 v3, 9, v118
	v_cndmask_b32_e32 v114, 0, v114, vcc
	v_cmp_lt_i32_e32 vcc, v118, v124
	s_nop 1
	v_cndmask_b32_e32 v116, 0, v116, vcc
	v_cmp_ge_i32_e32 vcc, v124, v2
	v_add_u32_e32 v2, 8, v118
	s_nop 0
	v_cndmask_b32_e32 v117, 0, v117, vcc
	v_cmp_le_i32_e32 vcc, v5, v124
	v_add_u32_e32 v5, 19, v118
	s_nop 0
	v_cndmask_b32_e32 v53, 0, v53, vcc
	v_cmp_le_i32_e32 vcc, v4, v124
	v_add_u32_e32 v4, 18, v118
	s_nop 0
	v_cndmask_b32_e32 v52, 0, v52, vcc
	v_cmp_le_i32_e32 vcc, v3, v124
	v_add_u32_e32 v3, 17, v118
	s_nop 0
	v_cndmask_b32_e32 v51, 0, v51, vcc
	v_cmp_le_i32_e32 vcc, v2, v124
	v_add_u32_e32 v2, 16, v118
	s_nop 0
	v_cndmask_b32_e32 v50, 0, v50, vcc
	v_cmp_le_i32_e32 vcc, v5, v124
	v_add_u32_e32 v5, 27, v118
	s_nop 0
	v_cndmask_b32_e32 v45, 0, v45, vcc
	v_cmp_le_i32_e32 vcc, v4, v124
	v_add_u32_e32 v4, 26, v118
	s_nop 0
	v_cndmask_b32_e32 v44, 0, v44, vcc
	v_cmp_le_i32_e32 vcc, v3, v124
	v_add_u32_e32 v3, 25, v118
	s_nop 0
	v_cndmask_b32_e32 v43, 0, v43, vcc
	v_cmp_le_i32_e32 vcc, v2, v124
	v_add_u32_e32 v2, 24, v118
	s_nop 0
	v_cndmask_b32_e32 v42, 0, v42, vcc
	v_cmp_le_i32_e32 vcc, v5, v124
	s_nop 1
	v_cndmask_b32_e32 v49, 0, v49, vcc
	v_cmp_le_i32_e32 vcc, v4, v124
	s_nop 1
	v_cndmask_b32_e32 v48, 0, v48, vcc
	v_cmp_le_i32_e32 vcc, v3, v124
	s_nop 1
	v_cndmask_b32_e32 v47, 0, v47, vcc
	v_cmp_le_i32_e32 vcc, v2, v124
	s_nop 1
	v_cndmask_b32_e32 v46, 0, v46, vcc

; __device__ __forceinline__ unsigned ordkey(float f) { const unsigned u = __float_as_uint(f); return u ^ ((unsigned)((int)u >> 31) | 0x80000000u); }
; __device__ __forceinline__ int crow(int r, int hi) { return (r & 3) + 8 * (r >> 2) + 4 * hi; }
; __global__ void __launch_bounds__(NWAVES * 64, 2) mega_fwd(Args args) {
;     ...
;                         for (int h = 0; h < 8; ++h) { fa::f32x16 a;
; #pragma unroll
;                             for (int r = 0; r < 16; ++r) a[r] = 0.f;
;                             a = __builtin_amdgcn_mfma_f32_32x32x16_f16(kf0, __builtin_bit_cast(f16x8, iqL[(2 * h) * 64 + lane]), a, 0, 0, 0);
;                             a = __builtin_amdgcn_mfma_f32_32x32x16_f16(kf1, __builtin_bit_cast(f16x8, iqL[(2 * h + 1) * 64 + lane]), a, 0, 0, 0);
;                             const float sg = ((sgnbits >> h) & 1u) ? -1.f : 1.f;
; #pragma unroll
;                             for (int r = 0; r < 16; ++r) sc[r] = __builtin_fmaf(__builtin_fabsf(a[r]), sg, sc[r]); }
; #pragma unroll
;                         for (int r = 0; r < 16; ++r) keys[ti][16 * half + r] = ordkey(sc[r]);
;                         if (k0 + 63 > 32 * qg) {
; #pragma unroll
;                             for (int r = 0; r < 16; ++r) { const int kidx = k0 + 32 * half + fa::crow(r, hi); keys[ti][16 * half + r] = (kidx <= t) ? keys[ti][16 * half + r] : 0u; } } }
.LBB0_625:
	ds_read_b128 v[18:21], v106
	ds_read_b128 v[102:105], v106 offset:1024
	ds_read_b128 v[224:227], v106 offset:2048
	ds_read_b128 v[176:179], v106 offset:3072
	s_waitcnt lgkmcnt(3)
	v_mfma_f32_32x32x16_f16 v[18:33], v[82:85], v[18:21], 0
	s_waitcnt lgkmcnt(2)
	v_mfma_f32_32x32x16_f16 v[18:33], v[62:65], v[102:105], v[18:33]
	s_waitcnt lgkmcnt(1)
	v_mfma_f32_32x32x16_f16 v[208:223], v[82:85], v[224:227], 0
	s_waitcnt lgkmcnt(0)
	v_mfma_f32_32x32x16_f16 v[208:223], v[62:65], v[176:179], v[208:223]
	v_bfe_u32 v102, v140, s26, 1
	v_cmp_eq_u32_e32 vcc, 0, v102
	v_lshrrev_b32_e32 v180, s26, v140
	v_and_b32_e32 v180, 2, v180
	v_cndmask_b32_e64 v102, -1.0, 1.0, vcc
	v_cmp_eq_u32_e32 vcc, 0, v180
	v_add_u32_e32 v106, 0x1000, v106
	s_add_i32 s26, s26, 2
	v_cndmask_b32_e64 v180, -1.0, 1.0, vcc
	s_cmp_lg_u32 s26, 8
	v_fma_f32 v104, |v18|, v102, v2
	v_fma_f32 v105, |v19|, v102, v3
	v_fma_f32 v108, |v20|, v102, v4
	v_fma_f32 v109, |v21|, v102, v5
	v_fma_f32 v22, |v22|, v102, v6
	v_fma_f32 v23, |v23|, v102, v7
	v_fma_f32 v24, |v24|, v102, v8
	v_fma_f32 v25, |v25|, v102, v9
	v_fma_f32 v26, |v26|, v102, v10
	v_fma_f32 v27, |v27|, v102, v11
	v_fma_f32 v28, |v28|, v102, v12
	v_fma_f32 v29, |v29|, v102, v13
	v_fma_f32 v30, |v30|, v102, v14
	v_fma_f32 v31, |v31|, v102, v15
	v_fma_f32 v32, |v32|, v102, v16
	v_fma_f32 v33, |v33|, v102, v17
	v_fma_f32 v4, |v210|, v180, v108
	v_fma_f32 v5, |v211|, v180, v109
	v_fma_f32 v2, |v208|, v180, v104
	v_fma_f32 v3, |v209|, v180, v105
	v_fma_f32 v8, |v214|, v180, v24
	v_fma_f32 v9, |v215|, v180, v25
	v_fma_f32 v6, |v212|, v180, v22
	v_fma_f32 v7, |v213|, v180, v23
	v_fma_f32 v12, |v218|, v180, v28
	v_fma_f32 v13, |v219|, v180, v29
	v_fma_f32 v10, |v216|, v180, v26
	v_fma_f32 v11, |v217|, v180, v27
	v_fma_f32 v16, |v222|, v180, v32
	v_fma_f32 v17, |v223|, v180, v33
	v_fma_f32 v14, |v220|, v180, v30
	v_fma_f32 v15, |v221|, v180, v31
	s_cbranch_scc1 .LBB0_625
	v_ashrrev_i32_e32 v18, 31, v2
	v_ashrrev_i32_e32 v19, 31, v3
	v_ashrrev_i32_e32 v20, 31, v4
	v_ashrrev_i32_e32 v21, 31, v5
	v_bitop3_b32 v134, v21, v5, s68 bitop3:0x36
	v_bitop3_b32 v138, v20, v4, s68 bitop3:0x36
	v_bitop3_b32 v136, v19, v3, s68 bitop3:0x36
	v_bitop3_b32 v139, v18, v2, s68 bitop3:0x36
	v_ashrrev_i32_e32 v2, 31, v6
	v_ashrrev_i32_e32 v3, 31, v7
	v_ashrrev_i32_e32 v4, 31, v8
	v_ashrrev_i32_e32 v5, 31, v9
	v_bitop3_b32 v131, v5, v9, s68 bitop3:0x36
	v_bitop3_b32 v133, v4, v8, s68 bitop3:0x36
	v_bitop3_b32 v137, v3, v7, s68 bitop3:0x36
	v_bitop3_b32 v135, v2, v6, s68 bitop3:0x36
	v_ashrrev_i32_e32 v2, 31, v10
	v_ashrrev_i32_e32 v3, 31, v11
	v_ashrrev_i32_e32 v4, 31, v12
	v_ashrrev_i32_e32 v5, 31, v13
	v_bitop3_b32 v129, v5, v13, s68 bitop3:0x36
	v_bitop3_b32 v126, v4, v12, s68 bitop3:0x36
	v_bitop3_b32 v127, v3, v11, s68 bitop3:0x36
	v_bitop3_b32 v132, v2, v10, s68 bitop3:0x36
	v_ashrrev_i32_e32 v2, 31, v14
	v_ashrrev_i32_e32 v3, 31, v15
	v_ashrrev_i32_e32 v4, 31, v16
	v_ashrrev_i32_e32 v5, 31, v17
	v_bitop3_b32 v62, v5, v17, s68 bitop3:0x36
	v_bitop3_b32 v125, v4, v16, s68 bitop3:0x36
	v_bitop3_b32 v128, v3, v15, s68 bitop3:0x36
	s_andn2_b64 vcc, exec, s[40:41]
	v_bitop3_b32 v130, v2, v14, s68 bitop3:0x36
	s_cbranch_vccnz .LBB0_628
	v_add_u32_e32 v2, 32, v118
	v_or_b32_e32 v4, 2, v2
	v_or_b32_e32 v3, 3, v2
	v_cmp_le_i32_e32 vcc, v4, v124
	v_add_u32_e32 v5, 40, v118
	v_add_u32_e32 v4, 41, v118
	v_cndmask_b32_e32 v138, 0, v138, vcc
	v_cmp_le_i32_e32 vcc, v3, v124
	v_add_u32_e32 v3, 42, v118
	s_nop 0
	v_cndmask_b32_e32 v134, 0, v134, vcc
	v_cmp_le_i32_e32 vcc, v2, v124
	s_nop 1
	v_cndmask_b32_e32 v139, 0, v139, vcc
	v_cmp_gt_i32_e32 vcc, v124, v2
	v_add_u32_e32 v2, 43, v118
	s_nop 0
	v_cndmask_b32_e32 v136, 0, v136, vcc
	v_cmp_le_i32_e32 vcc, v5, v124
	v_add_u32_e32 v5, 48, v118
	s_nop 0
	v_cndmask_b32_e32 v135, 0, v135, vcc
	v_cmp_le_i32_e32 vcc, v4, v124
	v_add_u32_e32 v4, 49, v118
	s_nop 0
	v_cndmask_b32_e32 v137, 0, v137, vcc
	v_cmp_le_i32_e32 vcc, v3, v124
	v_add_u32_e32 v3, 50, v118
	s_nop 0
	v_cndmask_b32_e32 v133, 0, v133, vcc
	v_cmp_le_i32_e32 vcc, v2, v124
	v_add_u32_e32 v2, 51, v118
	s_nop 0
	v_cndmask_b32_e32 v131, 0, v131, vcc
	v_cmp_le_i32_e32 vcc, v5, v124
	v_add_u32_e32 v5, 56, v118
	s_nop 0
	v_cndmask_b32_e32 v132, 0, v132, vcc
	v_cmp_le_i32_e32 vcc, v4, v124
	v_add_u32_e32 v4, 57, v118
	s_nop 0
	v_cndmask_b32_e32 v127, 0, v127, vcc
	v_cmp_le_i32_e32 vcc, v3, v124
	v_add_u32_e32 v3, 58, v118
	s_nop 0
	v_cndmask_b32_e32 v126, 0, v126, vcc
	v_cmp_le_i32_e32 vcc, v2, v124
	v_add_u32_e32 v2, 59, v118
	s_nop 0
	v_cndmask_b32_e32 v129, 0, v129, vcc
	v_cmp_le_i32_e32 vcc, v5, v124
	s_nop 1
	v_cndmask_b32_e32 v130, 0, v130, vcc
	v_cmp_le_i32_e32 vcc, v4, v124
	s_nop 1
	v_cndmask_b32_e32 v128, 0, v128, vcc
	v_cmp_le_i32_e32 vcc, v3, v124
	s_nop 1
	v_cndmask_b32_e32 v125, 0, v125, vcc
	v_cmp_le_i32_e32 vcc, v2, v124
	s_nop 1
	v_cndmask_b32_e32 v62, 0, v62, vcc

; __device__ __forceinline__ unsigned ordkey(float f) { const unsigned u = __float_as_uint(f); return u ^ ((unsigned)((int)u >> 31) | 0x80000000u); }
; __device__ __forceinline__ int crow(int r, int hi) { return (r & 3) + 8 * (r >> 2) + 4 * hi; }
; __global__ void __launch_bounds__(NWAVES * 64, 2) mega_fwd(Args args) {
;     ...
;                         for (int h = 0; h < 8; ++h) { fa::f32x16 a;
; #pragma unroll
;                             for (int r = 0; r < 16; ++r) a[r] = 0.f;
;                             a = __builtin_amdgcn_mfma_f32_32x32x16_f16(kf0, __builtin_bit_cast(f16x8, iqL[(2 * h) * 64 + lane]), a, 0, 0, 0);
;                             a = __builtin_amdgcn_mfma_f32_32x32x16_f16(kf1, __builtin_bit_cast(f16x8, iqL[(2 * h + 1) * 64 + lane]), a, 0, 0, 0);
;                             const float sg = ((sgnbits >> h) & 1u) ? -1.f : 1.f;
; #pragma unroll
;                             for (int r = 0; r < 16; ++r) sc[r] = __builtin_fmaf(__builtin_fabsf(a[r]), sg, sc[r]); }
; #pragma unroll
;                         for (int r = 0; r < 16; ++r) keys[ti][16 * half + r] = ordkey(sc[r]);
;                         if (k0 + 63 > 32 * qg) {
; #pragma unroll
;                             for (int r = 0; r < 16; ++r) { const int kidx = k0 + 32 * half + fa::crow(r, hi); keys[ti][16 * half + r] = (kidx <= t) ? keys[ti][16 * half + r] : 0u; } } }
.LBB0_630:
	ds_read_b128 v[18:21], v63
	ds_read_b128 v[82:85], v63 offset:1024
	ds_read_b128 v[224:227], v63 offset:2048
	ds_read_b128 v[176:179], v63 offset:3072
	s_waitcnt lgkmcnt(3)
	v_mfma_f32_32x32x16_f16 v[18:33], v[78:81], v[18:21], 0
	s_waitcnt lgkmcnt(2)
	v_mfma_f32_32x32x16_f16 v[18:33], v[74:77], v[82:85], v[18:33]
	s_waitcnt lgkmcnt(1)
	v_mfma_f32_32x32x16_f16 v[208:223], v[78:81], v[224:227], 0
	s_waitcnt lgkmcnt(0)
	v_mfma_f32_32x32x16_f16 v[208:223], v[74:77], v[176:179], v[208:223]
	v_bfe_u32 v4, v140, s26, 1
	v_cmp_eq_u32_e32 vcc, 0, v4
	v_lshrrev_b32_e32 v180, s26, v140
	v_and_b32_e32 v180, 2, v180
	v_cndmask_b32_e64 v4, -1.0, 1.0, vcc
	v_cmp_eq_u32_e32 vcc, 0, v180
	v_add_u32_e32 v63, 0x1000, v63
	s_add_i32 s26, s26, 2
	v_cndmask_b32_e64 v180, -1.0, 1.0, vcc
	s_cmp_lg_u32 s26, 8
	v_fma_f32 v64, |v20|, v4, v64
	v_fma_f32 v65, |v18|, v4, v65
	v_fma_f32 v82, |v19|, v4, v2
	v_fma_f32 v83, |v21|, v4, v3
	v_fma_f32 v22, |v22|, v4, v6
	v_fma_f32 v23, |v23|, v4, v7
	v_fma_f32 v24, |v24|, v4, v8
	v_fma_f32 v25, |v25|, v4, v9
	v_fma_f32 v26, |v26|, v4, v10
	v_fma_f32 v27, |v27|, v4, v11
	v_fma_f32 v28, |v28|, v4, v12
	v_fma_f32 v29, |v29|, v4, v13
	v_fma_f32 v30, |v30|, v4, v14
	v_fma_f32 v31, |v31|, v4, v15
	v_fma_f32 v32, |v32|, v4, v16
	v_fma_f32 v33, |v33|, v4, v17
	v_fma_f32 v64, |v210|, v180, v64
	v_fma_f32 v65, |v208|, v180, v65
	v_fma_f32 v2, |v209|, v180, v82
	v_fma_f32 v3, |v211|, v180, v83
	v_fma_f32 v8, |v214|, v180, v24
	v_fma_f32 v9, |v215|, v180, v25
	v_fma_f32 v6, |v212|, v180, v22
	v_fma_f32 v7, |v213|, v180, v23
	v_fma_f32 v12, |v218|, v180, v28
	v_fma_f32 v13, |v219|, v180, v29
	v_fma_f32 v10, |v216|, v180, v26
	v_fma_f32 v11, |v217|, v180, v27
	v_fma_f32 v16, |v222|, v180, v32
	v_fma_f32 v17, |v223|, v180, v33
	v_fma_f32 v14, |v220|, v180, v30
	v_fma_f32 v15, |v221|, v180, v31
	s_cbranch_scc1 .LBB0_630
	v_ashrrev_i32_e32 v4, 31, v65
	v_ashrrev_i32_e32 v5, 31, v64
	v_or_b32_e32 v4, 0x80000000, v4
	v_or_b32_e32 v5, 0x80000000, v5
	v_xor_b32_e32 v119, v4, v65
	v_xor_b32_e32 v118, v5, v64
	v_ashrrev_i32_e32 v4, 31, v3
	v_ashrrev_i32_e32 v5, 31, v2
	v_or_b32_e32 v4, 0x80000000, v4
	v_or_b32_e32 v5, 0x80000000, v5
	v_xor_b32_e32 v121, v4, v3
	v_xor_b32_e32 v120, v5, v2
	v_ashrrev_i32_e32 v2, 31, v6
	v_ashrrev_i32_e32 v3, 31, v7
	v_ashrrev_i32_e32 v4, 31, v8
	v_ashrrev_i32_e32 v5, 31, v9
	v_readlane_b32 s26, v254, 34
	v_bitop3_b32 v85, v5, v9, s68 bitop3:0x36
	v_bitop3_b32 v84, v4, v8, s68 bitop3:0x36
	v_bitop3_b32 v83, v3, v7, s68 bitop3:0x36
	v_bitop3_b32 v82, v2, v6, s68 bitop3:0x36
	v_ashrrev_i32_e32 v2, 31, v10
	v_ashrrev_i32_e32 v3, 31, v11
	v_ashrrev_i32_e32 v4, 31, v12
	v_ashrrev_i32_e32 v5, 31, v13
	s_cmp_gt_u32 s26, s44
	v_readlane_b32 s28, v253, 13
	v_bitop3_b32 v77, v5, v13, s68 bitop3:0x36
	v_bitop3_b32 v76, v4, v12, s68 bitop3:0x36
	v_bitop3_b32 v75, v3, v11, s68 bitop3:0x36
	v_bitop3_b32 v74, v2, v10, s68 bitop3:0x36
	v_ashrrev_i32_e32 v2, 31, v14
	v_ashrrev_i32_e32 v3, 31, v15
	v_ashrrev_i32_e32 v4, 31, v16
	v_ashrrev_i32_e32 v5, 31, v17
	s_cselect_b64 s[40:41], -1, 0
	s_cmp_le_u32 s26, s44
	v_add_u32_e32 v122, s28, v142
	v_bitop3_b32 v81, v5, v17, s68 bitop3:0x36
	v_bitop3_b32 v80, v4, v16, s68 bitop3:0x36
	v_bitop3_b32 v79, v3, v15, s68 bitop3:0x36
	v_bitop3_b32 v78, v2, v14, s68 bitop3:0x36
	v_readlane_b32 s29, v253, 14
	s_cbranch_scc1 .LBB0_633
	v_or_b32_e32 v2, 2, v122
	v_cmp_le_i32_e32 vcc, v122, v124
	v_add_u32_e32 v5, 11, v122
	v_add_u32_e32 v4, 10, v122
	v_cndmask_b32_e32 v119, 0, v119, vcc
	v_cmp_le_i32_e32 vcc, v2, v124
	v_or_b32_e32 v2, 3, v122
	v_add_u32_e32 v3, 9, v122
	v_cndmask_b32_e32 v118, 0, v118, vcc
	v_cmp_lt_i32_e32 vcc, v122, v124
	s_nop 1
	v_cndmask_b32_e32 v120, 0, v120, vcc
	v_cmp_ge_i32_e32 vcc, v124, v2
	v_add_u32_e32 v2, 8, v122
	s_nop 0
	v_cndmask_b32_e32 v121, 0, v121, vcc
	v_cmp_le_i32_e32 vcc, v5, v124
	v_add_u32_e32 v5, 19, v122
	s_nop 0
	v_cndmask_b32_e32 v85, 0, v85, vcc
	v_cmp_le_i32_e32 vcc, v4, v124
	v_add_u32_e32 v4, 18, v122
	s_nop 0
	v_cndmask_b32_e32 v84, 0, v84, vcc
	v_cmp_le_i32_e32 vcc, v3, v124
	v_add_u32_e32 v3, 17, v122
	s_nop 0
	v_cndmask_b32_e32 v83, 0, v83, vcc
	v_cmp_le_i32_e32 vcc, v2, v124
	v_add_u32_e32 v2, 16, v122
	s_nop 0
	v_cndmask_b32_e32 v82, 0, v82, vcc
	v_cmp_le_i32_e32 vcc, v5, v124
	v_add_u32_e32 v5, 27, v122
	s_nop 0
	v_cndmask_b32_e32 v77, 0, v77, vcc
	v_cmp_le_i32_e32 vcc, v4, v124
	v_add_u32_e32 v4, 26, v122
	s_nop 0
	v_cndmask_b32_e32 v76, 0, v76, vcc
	v_cmp_le_i32_e32 vcc, v3, v124
	v_add_u32_e32 v3, 25, v122
	s_nop 0
	v_cndmask_b32_e32 v75, 0, v75, vcc
	v_cmp_le_i32_e32 vcc, v2, v124
	v_add_u32_e32 v2, 24, v122
	s_nop 0
	v_cndmask_b32_e32 v74, 0, v74, vcc
	v_cmp_le_i32_e32 vcc, v5, v124
	s_nop 1
	v_cndmask_b32_e32 v81, 0, v81, vcc
	v_cmp_le_i32_e32 vcc, v4, v124
	s_nop 1
	v_cndmask_b32_e32 v80, 0, v80, vcc
	v_cmp_le_i32_e32 vcc, v3, v124
	s_nop 1
	v_cndmask_b32_e32 v79, 0, v79, vcc
	v_cmp_le_i32_e32 vcc, v2, v124
	s_nop 1
	v_cndmask_b32_e32 v78, 0, v78, vcc

; __device__ __forceinline__ unsigned ordkey(float f) { const unsigned u = __float_as_uint(f); return u ^ ((unsigned)((int)u >> 31) | 0x80000000u); }
; __device__ __forceinline__ int crow(int r, int hi) { return (r & 3) + 8 * (r >> 2) + 4 * hi; }
; __global__ void __launch_bounds__(NWAVES * 64, 2) mega_fwd(Args args) {
;     ...
;                         for (int h = 0; h < 8; ++h) { fa::f32x16 a;
; #pragma unroll
;                             for (int r = 0; r < 16; ++r) a[r] = 0.f;
;                             a = __builtin_amdgcn_mfma_f32_32x32x16_f16(kf0, __builtin_bit_cast(f16x8, iqL[(2 * h) * 64 + lane]), a, 0, 0, 0);
;                             a = __builtin_amdgcn_mfma_f32_32x32x16_f16(kf1, __builtin_bit_cast(f16x8, iqL[(2 * h + 1) * 64 + lane]), a, 0, 0, 0);
;                             const float sg = ((sgnbits >> h) & 1u) ? -1.f : 1.f;
; #pragma unroll
;                             for (int r = 0; r < 16; ++r) sc[r] = __builtin_fmaf(__builtin_fabsf(a[r]), sg, sc[r]); }
; #pragma unroll
;                         for (int r = 0; r < 16; ++r) keys[ti][16 * half + r] = ordkey(sc[r]);
;                         if (k0 + 63 > 32 * qg) {
; #pragma unroll
;                             for (int r = 0; r < 16; ++r) { const int kidx = k0 + 32 * half + fa::crow(r, hi); keys[ti][16 * half + r] = (kidx <= t) ? keys[ti][16 * half + r] : 0u; } } }
.LBB0_634:
	ds_read_b128 v[18:21], v63
	ds_read_b128 v[102:105], v63 offset:1024
	ds_read_b128 v[224:227], v63 offset:2048
	ds_read_b128 v[176:179], v63 offset:3072
	s_waitcnt lgkmcnt(3)
	v_mfma_f32_32x32x16_f16 v[18:33], v[98:101], v[18:21], 0
	s_waitcnt lgkmcnt(2)
	v_mfma_f32_32x32x16_f16 v[18:33], v[94:97], v[102:105], v[18:33]
	s_waitcnt lgkmcnt(1)
	v_mfma_f32_32x32x16_f16 v[208:223], v[98:101], v[224:227], 0
	s_waitcnt lgkmcnt(0)
	v_mfma_f32_32x32x16_f16 v[208:223], v[94:97], v[176:179], v[208:223]
	v_bfe_u32 v64, v140, s26, 1
	v_cmp_eq_u32_e32 vcc, 0, v64
	v_lshrrev_b32_e32 v180, s26, v140
	v_and_b32_e32 v180, 2, v180
	v_cndmask_b32_e64 v64, -1.0, 1.0, vcc
	v_cmp_eq_u32_e32 vcc, 0, v180
	v_add_u32_e32 v63, 0x1000, v63
	s_add_i32 s26, s26, 2
	v_cndmask_b32_e64 v180, -1.0, 1.0, vcc
	s_cmp_lg_u32 s26, 8
	v_fma_f32 v102, |v18|, v64, v2
	v_fma_f32 v103, |v19|, v64, v3
	v_fma_f32 v104, |v20|, v64, v4
	v_fma_f32 v105, |v21|, v64, v5
	v_fma_f32 v22, |v22|, v64, v6
	v_fma_f32 v23, |v23|, v64, v7
	v_fma_f32 v24, |v24|, v64, v8
	v_fma_f32 v25, |v25|, v64, v9
	v_fma_f32 v26, |v26|, v64, v10
	v_fma_f32 v27, |v27|, v64, v11
	v_fma_f32 v28, |v28|, v64, v12
	v_fma_f32 v29, |v29|, v64, v13
	v_fma_f32 v30, |v30|, v64, v14
	v_fma_f32 v31, |v31|, v64, v15
	v_fma_f32 v32, |v32|, v64, v16
	v_fma_f32 v33, |v33|, v64, v17
	v_fma_f32 v4, |v210|, v180, v104
	v_fma_f32 v5, |v211|, v180, v105
	v_fma_f32 v2, |v208|, v180, v102
	v_fma_f32 v3, |v209|, v180, v103
	v_fma_f32 v8, |v214|, v180, v24
	v_fma_f32 v9, |v215|, v180, v25
	v_fma_f32 v6, |v212|, v180, v22
	v_fma_f32 v7, |v213|, v180, v23
	v_fma_f32 v12, |v218|, v180, v28
	v_fma_f32 v13, |v219|, v180, v29
	v_fma_f32 v10, |v216|, v180, v26
	v_fma_f32 v11, |v217|, v180, v27
	v_fma_f32 v16, |v222|, v180, v32
	v_fma_f32 v17, |v223|, v180, v33
	v_fma_f32 v14, |v220|, v180, v30
	v_fma_f32 v15, |v221|, v180, v31
	s_cbranch_scc1 .LBB0_634
	v_ashrrev_i32_e32 v18, 31, v2
	v_ashrrev_i32_e32 v19, 31, v3
	v_ashrrev_i32_e32 v20, 31, v4
	v_ashrrev_i32_e32 v21, 31, v5
	v_bitop3_b32 v151, v21, v5, s68 bitop3:0x36
	v_bitop3_b32 v155, v20, v4, s68 bitop3:0x36
	v_bitop3_b32 v153, v19, v3, s68 bitop3:0x36
	v_bitop3_b32 v156, v18, v2, s68 bitop3:0x36
	v_ashrrev_i32_e32 v2, 31, v6
	v_ashrrev_i32_e32 v3, 31, v7
	v_ashrrev_i32_e32 v4, 31, v8
	v_ashrrev_i32_e32 v5, 31, v9
	v_bitop3_b32 v148, v5, v9, s68 bitop3:0x36
	v_bitop3_b32 v150, v4, v8, s68 bitop3:0x36
	v_bitop3_b32 v154, v3, v7, s68 bitop3:0x36
	v_bitop3_b32 v152, v2, v6, s68 bitop3:0x36
	v_ashrrev_i32_e32 v2, 31, v10
	v_ashrrev_i32_e32 v3, 31, v11
	v_ashrrev_i32_e32 v4, 31, v12
	v_ashrrev_i32_e32 v5, 31, v13
	v_bitop3_b32 v146, v5, v13, s68 bitop3:0x36
	v_bitop3_b32 v143, v4, v12, s68 bitop3:0x36
	v_bitop3_b32 v144, v3, v11, s68 bitop3:0x36
	v_bitop3_b32 v149, v2, v10, s68 bitop3:0x36
	v_ashrrev_i32_e32 v2, 31, v14
	v_ashrrev_i32_e32 v3, 31, v15
	v_ashrrev_i32_e32 v4, 31, v16
	v_ashrrev_i32_e32 v5, 31, v17
	v_bitop3_b32 v94, v5, v17, s68 bitop3:0x36
	v_bitop3_b32 v63, v4, v16, s68 bitop3:0x36
	v_bitop3_b32 v145, v3, v15, s68 bitop3:0x36
	s_andn2_b64 vcc, exec, s[40:41]
	v_bitop3_b32 v147, v2, v14, s68 bitop3:0x36
	s_cbranch_vccnz .LBB0_637
	v_add_u32_e32 v2, 32, v122
	v_or_b32_e32 v4, 2, v2
	v_or_b32_e32 v3, 3, v2
	v_cmp_le_i32_e32 vcc, v4, v124
	v_add_u32_e32 v5, 40, v122
	v_add_u32_e32 v4, 41, v122
	v_cndmask_b32_e32 v155, 0, v155, vcc
	v_cmp_le_i32_e32 vcc, v3, v124
	v_add_u32_e32 v3, 42, v122
	s_nop 0
	v_cndmask_b32_e32 v151, 0, v151, vcc
	v_cmp_le_i32_e32 vcc, v2, v124
	s_nop 1
	v_cndmask_b32_e32 v156, 0, v156, vcc
	v_cmp_gt_i32_e32 vcc, v124, v2
	v_add_u32_e32 v2, 43, v122
	s_nop 0
	v_cndmask_b32_e32 v153, 0, v153, vcc
	v_cmp_le_i32_e32 vcc, v5, v124
	v_add_u32_e32 v5, 48, v122
	s_nop 0
	v_cndmask_b32_e32 v152, 0, v152, vcc
	v_cmp_le_i32_e32 vcc, v4, v124
	v_add_u32_e32 v4, 49, v122
	s_nop 0
	v_cndmask_b32_e32 v154, 0, v154, vcc
	v_cmp_le_i32_e32 vcc, v3, v124
	v_add_u32_e32 v3, 50, v122
	s_nop 0
	v_cndmask_b32_e32 v150, 0, v150, vcc
	v_cmp_le_i32_e32 vcc, v2, v124
	v_add_u32_e32 v2, 51, v122
	s_nop 0
	v_cndmask_b32_e32 v148, 0, v148, vcc
	v_cmp_le_i32_e32 vcc, v5, v124
	v_add_u32_e32 v5, 56, v122
	s_nop 0
	v_cndmask_b32_e32 v149, 0, v149, vcc
	v_cmp_le_i32_e32 vcc, v4, v124
	v_add_u32_e32 v4, 57, v122
	s_nop 0
	v_cndmask_b32_e32 v144, 0, v144, vcc
	v_cmp_le_i32_e32 vcc, v3, v124
	v_add_u32_e32 v3, 58, v122
	s_nop 0
	v_cndmask_b32_e32 v143, 0, v143, vcc
	v_cmp_le_i32_e32 vcc, v2, v124
	v_add_u32_e32 v2, 59, v122
	s_nop 0
	v_cndmask_b32_e32 v146, 0, v146, vcc
	v_cmp_le_i32_e32 vcc, v5, v124
	s_nop 1
	v_cndmask_b32_e32 v147, 0, v147, vcc
	v_cmp_le_i32_e32 vcc, v4, v124
	s_nop 1
	v_cndmask_b32_e32 v145, 0, v145, vcc
	v_cmp_le_i32_e32 vcc, v3, v124
	s_nop 1
	v_cndmask_b32_e32 v63, 0, v63, vcc
	v_cmp_le_i32_e32 vcc, v2, v124
	s_nop 1
	v_cndmask_b32_e32 v94, 0, v94, vcc

; __device__ __forceinline__ unsigned ordkey(float f) { const unsigned u = __float_as_uint(f); return u ^ ((unsigned)((int)u >> 31) | 0x80000000u); }
; __device__ __forceinline__ int crow(int r, int hi) { return (r & 3) + 8 * (r >> 2) + 4 * hi; }
; __global__ void __launch_bounds__(NWAVES * 64, 2) mega_fwd(Args args) {
;     ...
;                         for (int h = 0; h < 8; ++h) { fa::f32x16 a;
; #pragma unroll
;                             for (int r = 0; r < 16; ++r) a[r] = 0.f;
;                             a = __builtin_amdgcn_mfma_f32_32x32x16_f16(kf0, __builtin_bit_cast(f16x8, iqL[(2 * h) * 64 + lane]), a, 0, 0, 0);
;                             a = __builtin_amdgcn_mfma_f32_32x32x16_f16(kf1, __builtin_bit_cast(f16x8, iqL[(2 * h + 1) * 64 + lane]), a, 0, 0, 0);
;                             const float sg = ((sgnbits >> h) & 1u) ? -1.f : 1.f;
; #pragma unroll
;                             for (int r = 0; r < 16; ++r) sc[r] = __builtin_fmaf(__builtin_fabsf(a[r]), sg, sc[r]); }
; #pragma unroll
;                         for (int r = 0; r < 16; ++r) keys[ti][16 * half + r] = ordkey(sc[r]);
;                         if (k0 + 63 > 32 * qg) {
; #pragma unroll
;                             for (int r = 0; r < 16; ++r) { const int kidx = k0 + 32 * half + fa::crow(r, hi); keys[ti][16 * half + r] = (kidx <= t) ? keys[ti][16 * half + r] : 0u; } } }
.LBB0_639:
	ds_read_b128 v[18:21], v95
	ds_read_b128 v[96:99], v95 offset:1024
	ds_read_b128 v[224:227], v95 offset:2048
	ds_read_b128 v[176:179], v95 offset:3072
	s_waitcnt lgkmcnt(3)
	v_mfma_f32_32x32x16_f16 v[18:33], v[90:93], v[18:21], 0
	s_waitcnt lgkmcnt(2)
	v_mfma_f32_32x32x16_f16 v[18:33], v[86:89], v[96:99], v[18:33]
	s_waitcnt lgkmcnt(1)
	v_mfma_f32_32x32x16_f16 v[208:223], v[90:93], v[224:227], 0
	s_waitcnt lgkmcnt(0)
	v_mfma_f32_32x32x16_f16 v[208:223], v[86:89], v[176:179], v[208:223]
	v_bfe_u32 v4, v140, s26, 1
	v_cmp_eq_u32_e32 vcc, 0, v4
	v_lshrrev_b32_e32 v180, s26, v140
	v_and_b32_e32 v180, 2, v180
	v_cndmask_b32_e64 v4, -1.0, 1.0, vcc
	v_cmp_eq_u32_e32 vcc, 0, v180
	v_add_u32_e32 v95, 0x1000, v95
	s_add_i32 s26, s26, 2
	v_cndmask_b32_e64 v180, -1.0, 1.0, vcc
	s_cmp_lg_u32 s26, 8
	v_fma_f32 v64, |v20|, v4, v64
	v_fma_f32 v65, |v18|, v4, v65
	v_fma_f32 v96, |v19|, v4, v2
	v_fma_f32 v97, |v21|, v4, v3
	v_fma_f32 v22, |v22|, v4, v6
	v_fma_f32 v23, |v23|, v4, v7
	v_fma_f32 v24, |v24|, v4, v8
	v_fma_f32 v25, |v25|, v4, v9
	v_fma_f32 v26, |v26|, v4, v10
	v_fma_f32 v27, |v27|, v4, v11
	v_fma_f32 v28, |v28|, v4, v12
	v_fma_f32 v29, |v29|, v4, v13
	v_fma_f32 v30, |v30|, v4, v14
	v_fma_f32 v31, |v31|, v4, v15
	v_fma_f32 v32, |v32|, v4, v16
	v_fma_f32 v33, |v33|, v4, v17
	v_fma_f32 v64, |v210|, v180, v64
	v_fma_f32 v65, |v208|, v180, v65
	v_fma_f32 v2, |v209|, v180, v96
	v_fma_f32 v3, |v211|, v180, v97
	v_fma_f32 v8, |v214|, v180, v24
	v_fma_f32 v9, |v215|, v180, v25
	v_fma_f32 v6, |v212|, v180, v22
	v_fma_f32 v7, |v213|, v180, v23
	v_fma_f32 v12, |v218|, v180, v28
	v_fma_f32 v13, |v219|, v180, v29
	v_fma_f32 v10, |v216|, v180, v26
	v_fma_f32 v11, |v217|, v180, v27
	v_fma_f32 v16, |v222|, v180, v32
	v_fma_f32 v17, |v223|, v180, v33
	v_fma_f32 v14, |v220|, v180, v30
	v_fma_f32 v15, |v221|, v180, v31
	s_cbranch_scc1 .LBB0_639
	v_ashrrev_i32_e32 v4, 31, v65
	v_ashrrev_i32_e32 v5, 31, v64
	v_or_b32_e32 v4, 0x80000000, v4
	v_or_b32_e32 v5, 0x80000000, v5
	v_xor_b32_e32 v109, v4, v65
	v_xor_b32_e32 v108, v5, v64
	v_ashrrev_i32_e32 v4, 31, v3
	v_ashrrev_i32_e32 v5, 31, v2
	v_or_b32_e32 v4, 0x80000000, v4
	v_or_b32_e32 v5, 0x80000000, v5
	v_xor_b32_e32 v123, v4, v3
	v_xor_b32_e32 v122, v5, v2
	v_ashrrev_i32_e32 v2, 31, v6
	v_ashrrev_i32_e32 v3, 31, v7
	v_ashrrev_i32_e32 v4, 31, v8
	v_ashrrev_i32_e32 v5, 31, v9
	v_readlane_b32 s26, v254, 35
	v_bitop3_b32 v99, v5, v9, s68 bitop3:0x36
	v_bitop3_b32 v98, v4, v8, s68 bitop3:0x36
	v_bitop3_b32 v97, v3, v7, s68 bitop3:0x36
	v_bitop3_b32 v96, v2, v6, s68 bitop3:0x36
	v_ashrrev_i32_e32 v2, 31, v10
	v_ashrrev_i32_e32 v3, 31, v11
	v_ashrrev_i32_e32 v4, 31, v12
	v_ashrrev_i32_e32 v5, 31, v13
	s_cmp_gt_u32 s26, s44
	v_readlane_b32 s28, v253, 39
	v_bitop3_b32 v89, v5, v13, s68 bitop3:0x36
	v_bitop3_b32 v88, v4, v12, s68 bitop3:0x36
	v_bitop3_b32 v87, v3, v11, s68 bitop3:0x36
	v_bitop3_b32 v86, v2, v10, s68 bitop3:0x36
	v_ashrrev_i32_e32 v2, 31, v14
	v_ashrrev_i32_e32 v3, 31, v15
	v_ashrrev_i32_e32 v4, 31, v16
	v_ashrrev_i32_e32 v5, 31, v17
	s_cselect_b64 s[40:41], -1, 0
	s_cmp_le_u32 s26, s44
	v_add_u32_e32 v171, s28, v142
	v_bitop3_b32 v93, v5, v17, s68 bitop3:0x36
	v_bitop3_b32 v92, v4, v16, s68 bitop3:0x36
	v_bitop3_b32 v91, v3, v15, s68 bitop3:0x36
	v_bitop3_b32 v90, v2, v14, s68 bitop3:0x36
	v_readlane_b32 s29, v253, 40
	s_cbranch_scc1 .LBB0_642
	v_or_b32_e32 v2, 2, v171
	v_cmp_le_i32_e32 vcc, v171, v124
	v_add_u32_e32 v5, 11, v171
	v_add_u32_e32 v4, 10, v171
	v_cndmask_b32_e32 v109, 0, v109, vcc
	v_cmp_le_i32_e32 vcc, v2, v124
	v_or_b32_e32 v2, 3, v171
	v_add_u32_e32 v3, 9, v171
	v_cndmask_b32_e32 v108, 0, v108, vcc
	v_cmp_lt_i32_e32 vcc, v171, v124
	s_nop 1
	v_cndmask_b32_e32 v122, 0, v122, vcc
	v_cmp_ge_i32_e32 vcc, v124, v2
	v_add_u32_e32 v2, 8, v171
	s_nop 0
	v_cndmask_b32_e32 v123, 0, v123, vcc
	v_cmp_le_i32_e32 vcc, v5, v124
	v_add_u32_e32 v5, 19, v171
	s_nop 0
	v_cndmask_b32_e32 v99, 0, v99, vcc
	v_cmp_le_i32_e32 vcc, v4, v124
	v_add_u32_e32 v4, 18, v171
	s_nop 0
	v_cndmask_b32_e32 v98, 0, v98, vcc
	v_cmp_le_i32_e32 vcc, v3, v124
	v_add_u32_e32 v3, 17, v171
	s_nop 0
	v_cndmask_b32_e32 v97, 0, v97, vcc
	v_cmp_le_i32_e32 vcc, v2, v124
	v_add_u32_e32 v2, 16, v171
	s_nop 0
	v_cndmask_b32_e32 v96, 0, v96, vcc
	v_cmp_le_i32_e32 vcc, v5, v124
	v_add_u32_e32 v5, 27, v171
	s_nop 0
	v_cndmask_b32_e32 v89, 0, v89, vcc
	v_cmp_le_i32_e32 vcc, v4, v124
	v_add_u32_e32 v4, 26, v171
	s_nop 0
	v_cndmask_b32_e32 v88, 0, v88, vcc
	v_cmp_le_i32_e32 vcc, v3, v124
	v_add_u32_e32 v3, 25, v171
	s_nop 0
	v_cndmask_b32_e32 v87, 0, v87, vcc
	v_cmp_le_i32_e32 vcc, v2, v124
	v_add_u32_e32 v2, 24, v171
	s_nop 0
	v_cndmask_b32_e32 v86, 0, v86, vcc
	v_cmp_le_i32_e32 vcc, v5, v124
	s_nop 1
	v_cndmask_b32_e32 v93, 0, v93, vcc
	v_cmp_le_i32_e32 vcc, v4, v124
	s_nop 1
	v_cndmask_b32_e32 v92, 0, v92, vcc
	v_cmp_le_i32_e32 vcc, v3, v124
	s_nop 1
	v_cndmask_b32_e32 v91, 0, v91, vcc
	v_cmp_le_i32_e32 vcc, v2, v124
	s_nop 1
	v_cndmask_b32_e32 v90, 0, v90, vcc

; __device__ __forceinline__ unsigned ordkey(float f) { const unsigned u = __float_as_uint(f); return u ^ ((unsigned)((int)u >> 31) | 0x80000000u); }
; __device__ __forceinline__ int crow(int r, int hi) { return (r & 3) + 8 * (r >> 2) + 4 * hi; }
; __global__ void __launch_bounds__(NWAVES * 64, 2) mega_fwd(Args args) {
;     ...
;                         for (int h = 0; h < 8; ++h) { fa::f32x16 a;
; #pragma unroll
;                             for (int r = 0; r < 16; ++r) a[r] = 0.f;
;                             a = __builtin_amdgcn_mfma_f32_32x32x16_f16(kf0, __builtin_bit_cast(f16x8, iqL[(2 * h) * 64 + lane]), a, 0, 0, 0);
;                             a = __builtin_amdgcn_mfma_f32_32x32x16_f16(kf1, __builtin_bit_cast(f16x8, iqL[(2 * h + 1) * 64 + lane]), a, 0, 0, 0);
;                             const float sg = ((sgnbits >> h) & 1u) ? -1.f : 1.f;
; #pragma unroll
;                             for (int r = 0; r < 16; ++r) sc[r] = __builtin_fmaf(__builtin_fabsf(a[r]), sg, sc[r]); }
; #pragma unroll
;                         for (int r = 0; r < 16; ++r) keys[ti][16 * half + r] = ordkey(sc[r]);
;                         if (k0 + 63 > 32 * qg) {
; #pragma unroll
;                             for (int r = 0; r < 16; ++r) { const int kidx = k0 + 32 * half + fa::crow(r, hi); keys[ti][16 * half + r] = (kidx <= t) ? keys[ti][16 * half + r] : 0u; } } }
.LBB0_643:
	ds_read_b128 v[18:21], v64
	ds_read_b128 v[100:103], v64 offset:1024
	ds_read_b128 v[224:227], v64 offset:2048
	ds_read_b128 v[176:179], v64 offset:3072
	s_waitcnt lgkmcnt(3)
	v_mfma_f32_32x32x16_f16 v[18:33], v[70:73], v[18:21], 0
	s_waitcnt lgkmcnt(2)
	v_mfma_f32_32x32x16_f16 v[18:33], v[66:69], v[100:103], v[18:33]
	s_waitcnt lgkmcnt(1)
	v_mfma_f32_32x32x16_f16 v[208:223], v[70:73], v[224:227], 0
	s_waitcnt lgkmcnt(0)
	v_mfma_f32_32x32x16_f16 v[208:223], v[66:69], v[176:179], v[208:223]
	v_bfe_u32 v100, v140, s26, 1
	v_cmp_eq_u32_e32 vcc, 0, v100
	v_lshrrev_b32_e32 v180, s26, v140
	v_and_b32_e32 v180, 2, v180
	v_cndmask_b32_e64 v100, -1.0, 1.0, vcc
	v_cmp_eq_u32_e32 vcc, 0, v180
	v_add_u32_e32 v64, 0x1000, v64
	s_add_i32 s26, s26, 2
	v_cndmask_b32_e64 v180, -1.0, 1.0, vcc
	s_cmp_lg_u32 s26, 8
	v_fma_f32 v102, |v18|, v100, v2
	v_fma_f32 v103, |v19|, v100, v3
	v_fma_f32 v104, |v20|, v100, v4
	v_fma_f32 v105, |v21|, v100, v5
	v_fma_f32 v22, |v22|, v100, v6
	v_fma_f32 v23, |v23|, v100, v7
	v_fma_f32 v24, |v24|, v100, v8
	v_fma_f32 v25, |v25|, v100, v9
	v_fma_f32 v26, |v26|, v100, v10
	v_fma_f32 v27, |v27|, v100, v11
	v_fma_f32 v28, |v28|, v100, v12
	v_fma_f32 v29, |v29|, v100, v13
	v_fma_f32 v30, |v30|, v100, v14
	v_fma_f32 v31, |v31|, v100, v15
	v_fma_f32 v32, |v32|, v100, v16
	v_fma_f32 v33, |v33|, v100, v17
	v_fma_f32 v4, |v210|, v180, v104
	v_fma_f32 v5, |v211|, v180, v105
	v_fma_f32 v2, |v208|, v180, v102
	v_fma_f32 v3, |v209|, v180, v103
	v_fma_f32 v8, |v214|, v180, v24
	v_fma_f32 v9, |v215|, v180, v25
	v_fma_f32 v6, |v212|, v180, v22
	v_fma_f32 v7, |v213|, v180, v23
	v_fma_f32 v12, |v218|, v180, v28
	v_fma_f32 v13, |v219|, v180, v29
	v_fma_f32 v10, |v216|, v180, v26
	v_fma_f32 v11, |v217|, v180, v27
	v_fma_f32 v16, |v222|, v180, v32
	v_fma_f32 v17, |v223|, v180, v33
	v_fma_f32 v14, |v220|, v180, v30
	v_fma_f32 v15, |v221|, v180, v31
	s_cbranch_scc1 .LBB0_643
	v_ashrrev_i32_e32 v18, 31, v2
	v_ashrrev_i32_e32 v19, 31, v3
	v_ashrrev_i32_e32 v20, 31, v4
	v_ashrrev_i32_e32 v21, 31, v5
	v_bitop3_b32 v165, v21, v5, s68 bitop3:0x36
	v_bitop3_b32 v169, v20, v4, s68 bitop3:0x36
	v_bitop3_b32 v167, v19, v3, s68 bitop3:0x36
	v_bitop3_b32 v170, v18, v2, s68 bitop3:0x36
	v_ashrrev_i32_e32 v2, 31, v6
	v_ashrrev_i32_e32 v3, 31, v7
	v_ashrrev_i32_e32 v4, 31, v8
	v_ashrrev_i32_e32 v5, 31, v9
	v_bitop3_b32 v162, v5, v9, s68 bitop3:0x36
	v_bitop3_b32 v164, v4, v8, s68 bitop3:0x36
	v_bitop3_b32 v168, v3, v7, s68 bitop3:0x36
	v_bitop3_b32 v166, v2, v6, s68 bitop3:0x36
	v_ashrrev_i32_e32 v2, 31, v10
	v_ashrrev_i32_e32 v3, 31, v11
	v_ashrrev_i32_e32 v4, 31, v12
	v_ashrrev_i32_e32 v5, 31, v13
	v_bitop3_b32 v160, v5, v13, s68 bitop3:0x36
	v_bitop3_b32 v157, v4, v12, s68 bitop3:0x36
	v_bitop3_b32 v158, v3, v11, s68 bitop3:0x36
	v_bitop3_b32 v163, v2, v10, s68 bitop3:0x36
	v_ashrrev_i32_e32 v2, 31, v14
	v_ashrrev_i32_e32 v3, 31, v15
	v_ashrrev_i32_e32 v4, 31, v16
	v_ashrrev_i32_e32 v5, 31, v17
	v_bitop3_b32 v64, v5, v17, s68 bitop3:0x36
	v_bitop3_b32 v95, v4, v16, s68 bitop3:0x36
	v_bitop3_b32 v159, v3, v15, s68 bitop3:0x36
	s_andn2_b64 vcc, exec, s[40:41]
	v_bitop3_b32 v161, v2, v14, s68 bitop3:0x36
	s_cbranch_vccnz .LBB0_646
	v_add_u32_e32 v2, 32, v171
	v_or_b32_e32 v4, 2, v2
	v_or_b32_e32 v3, 3, v2
	v_cmp_le_i32_e32 vcc, v4, v124
	v_add_u32_e32 v5, 40, v171
	v_add_u32_e32 v4, 41, v171
	v_cndmask_b32_e32 v169, 0, v169, vcc
	v_cmp_le_i32_e32 vcc, v3, v124
	v_add_u32_e32 v3, 42, v171
	s_nop 0
	v_cndmask_b32_e32 v165, 0, v165, vcc
	v_cmp_le_i32_e32 vcc, v2, v124
	s_nop 1
	v_cndmask_b32_e32 v170, 0, v170, vcc
	v_cmp_gt_i32_e32 vcc, v124, v2
	v_add_u32_e32 v2, 43, v171
	s_nop 0
	v_cndmask_b32_e32 v167, 0, v167, vcc
	v_cmp_le_i32_e32 vcc, v5, v124
	v_add_u32_e32 v5, 48, v171
	s_nop 0
	v_cndmask_b32_e32 v166, 0, v166, vcc
	v_cmp_le_i32_e32 vcc, v4, v124
	v_add_u32_e32 v4, 49, v171
	s_nop 0
	v_cndmask_b32_e32 v168, 0, v168, vcc
	v_cmp_le_i32_e32 vcc, v3, v124
	v_add_u32_e32 v3, 50, v171
	s_nop 0
	v_cndmask_b32_e32 v164, 0, v164, vcc
	v_cmp_le_i32_e32 vcc, v2, v124
	v_add_u32_e32 v2, 51, v171
	s_nop 0
	v_cndmask_b32_e32 v162, 0, v162, vcc
	v_cmp_le_i32_e32 vcc, v5, v124
	v_add_u32_e32 v5, 56, v171
	s_nop 0
	v_cndmask_b32_e32 v163, 0, v163, vcc
	v_cmp_le_i32_e32 vcc, v4, v124
	v_add_u32_e32 v4, 57, v171
	s_nop 0
	v_cndmask_b32_e32 v158, 0, v158, vcc
	v_cmp_le_i32_e32 vcc, v3, v124
	v_add_u32_e32 v3, 58, v171
	s_nop 0
	v_cndmask_b32_e32 v157, 0, v157, vcc
	v_cmp_le_i32_e32 vcc, v2, v124
	v_add_u32_e32 v2, 59, v171
	s_nop 0
	v_cndmask_b32_e32 v160, 0, v160, vcc
	v_cmp_le_i32_e32 vcc, v5, v124
	s_nop 1
	v_cndmask_b32_e32 v161, 0, v161, vcc
	v_cmp_le_i32_e32 vcc, v4, v124
	s_nop 1
	v_cndmask_b32_e32 v159, 0, v159, vcc
	v_cmp_le_i32_e32 vcc, v3, v124
	s_nop 1
	v_cndmask_b32_e32 v95, 0, v95, vcc
	v_cmp_le_i32_e32 vcc, v2, v124
	s_nop 1
	v_cndmask_b32_e32 v64, 0, v64, vcc

; __device__ __forceinline__ unsigned ordkey(float f) { const unsigned u = __float_as_uint(f); return u ^ ((unsigned)((int)u >> 31) | 0x80000000u); }
; __device__ __forceinline__ int crow(int r, int hi) { return (r & 3) + 8 * (r >> 2) + 4 * hi; }
; __global__ void __launch_bounds__(NWAVES * 64, 2) mega_fwd(Args args) {
;     ...
;                         for (int h = 0; h < 8; ++h) { fa::f32x16 a;
; #pragma unroll
;                             for (int r = 0; r < 16; ++r) a[r] = 0.f;
;                             a = __builtin_amdgcn_mfma_f32_32x32x16_f16(kf0, __builtin_bit_cast(f16x8, iqL[(2 * h) * 64 + lane]), a, 0, 0, 0);
;                             a = __builtin_amdgcn_mfma_f32_32x32x16_f16(kf1, __builtin_bit_cast(f16x8, iqL[(2 * h + 1) * 64 + lane]), a, 0, 0, 0);
;                             const float sg = ((sgnbits >> h) & 1u) ? -1.f : 1.f;
; #pragma unroll
;                             for (int r = 0; r < 16; ++r) sc[r] = __builtin_fmaf(__builtin_fabsf(a[r]), sg, sc[r]); }
; #pragma unroll
;                         for (int r = 0; r < 16; ++r) keys[ti][16 * half + r] = ordkey(sc[r]);
;                         if (k0 + 63 > 32 * qg) {
; #pragma unroll
;                             for (int r = 0; r < 16; ++r) { const int kidx = k0 + 32 * half + fa::crow(r, hi); keys[ti][16 * half + r] = (kidx <= t) ? keys[ti][16 * half + r] : 0u; } } }
.LBB0_648:
	ds_read_b128 v[18:21], v65
	ds_read_b128 v[104:107], v65 offset:1024
	ds_read_b128 v[224:227], v65 offset:2048
	ds_read_b128 v[176:179], v65 offset:3072
	s_waitcnt lgkmcnt(3)
	v_mfma_f32_32x32x16_f16 v[18:33], v[58:61], v[18:21], 0
	s_waitcnt lgkmcnt(2)
	v_mfma_f32_32x32x16_f16 v[18:33], v[54:57], v[104:107], v[18:33]
	s_waitcnt lgkmcnt(1)
	v_mfma_f32_32x32x16_f16 v[208:223], v[58:61], v[224:227], 0
	s_waitcnt lgkmcnt(0)
	v_mfma_f32_32x32x16_f16 v[208:223], v[54:57], v[176:179], v[208:223]
	v_bfe_u32 v4, v140, s26, 1
	v_cmp_eq_u32_e32 vcc, 0, v4
	v_lshrrev_b32_e32 v180, s26, v140
	v_and_b32_e32 v180, 2, v180
	v_cndmask_b32_e64 v4, -1.0, 1.0, vcc
	v_cmp_eq_u32_e32 vcc, 0, v180
	v_add_u32_e32 v65, 0x1000, v65
	s_add_i32 s26, s26, 2
	v_cndmask_b32_e64 v180, -1.0, 1.0, vcc
	s_cmp_lg_u32 s26, 8
	v_fma_f32 v66, |v20|, v4, v66
	v_fma_f32 v67, |v18|, v4, v67
	v_fma_f32 v68, |v19|, v4, v2
	v_fma_f32 v69, |v21|, v4, v3
	v_fma_f32 v22, |v22|, v4, v6
	v_fma_f32 v23, |v23|, v4, v7
	v_fma_f32 v24, |v24|, v4, v8
	v_fma_f32 v25, |v25|, v4, v9
	v_fma_f32 v26, |v26|, v4, v10
	v_fma_f32 v27, |v27|, v4, v11
	v_fma_f32 v28, |v28|, v4, v12
	v_fma_f32 v29, |v29|, v4, v13
	v_fma_f32 v30, |v30|, v4, v14
	v_fma_f32 v31, |v31|, v4, v15
	v_fma_f32 v32, |v32|, v4, v16
	v_fma_f32 v33, |v33|, v4, v17
	v_fma_f32 v66, |v210|, v180, v66
	v_fma_f32 v67, |v208|, v180, v67
	v_fma_f32 v2, |v209|, v180, v68
	v_fma_f32 v3, |v211|, v180, v69
	v_fma_f32 v8, |v214|, v180, v24
	v_fma_f32 v9, |v215|, v180, v25
	v_fma_f32 v6, |v212|, v180, v22
	v_fma_f32 v7, |v213|, v180, v23
	v_fma_f32 v12, |v218|, v180, v28
	v_fma_f32 v13, |v219|, v180, v29
	v_fma_f32 v10, |v216|, v180, v26
	v_fma_f32 v11, |v217|, v180, v27
	v_fma_f32 v16, |v222|, v180, v32
	v_fma_f32 v17, |v223|, v180, v33
	v_fma_f32 v14, |v220|, v180, v30
	v_fma_f32 v15, |v221|, v180, v31
	s_cbranch_scc1 .LBB0_648
	v_ashrrev_i32_e32 v4, 31, v67
	v_ashrrev_i32_e32 v5, 31, v66
	v_or_b32_e32 v4, 0x80000000, v4
	v_or_b32_e32 v5, 0x80000000, v5
	v_xor_b32_e32 v105, v4, v67
	v_xor_b32_e32 v104, v5, v66
	v_ashrrev_i32_e32 v4, 31, v3
	v_ashrrev_i32_e32 v5, 31, v2
	v_or_b32_e32 v4, 0x80000000, v4
	v_or_b32_e32 v5, 0x80000000, v5
	v_xor_b32_e32 v107, v4, v3
	v_xor_b32_e32 v106, v5, v2
	v_ashrrev_i32_e32 v2, 31, v6
	v_ashrrev_i32_e32 v3, 31, v7
	v_ashrrev_i32_e32 v4, 31, v8
	v_ashrrev_i32_e32 v5, 31, v9
	v_readlane_b32 s26, v254, 36
	v_bitop3_b32 v69, v5, v9, s68 bitop3:0x36
	v_bitop3_b32 v68, v4, v8, s68 bitop3:0x36
	v_bitop3_b32 v67, v3, v7, s68 bitop3:0x36
	v_bitop3_b32 v66, v2, v6, s68 bitop3:0x36
	v_ashrrev_i32_e32 v2, 31, v10
	v_ashrrev_i32_e32 v3, 31, v11
	v_ashrrev_i32_e32 v4, 31, v12
	v_ashrrev_i32_e32 v5, 31, v13
	s_cmp_gt_u32 s26, s44
	v_readlane_b32 s28, v253, 4
	v_bitop3_b32 v57, v5, v13, s68 bitop3:0x36
	v_bitop3_b32 v56, v4, v12, s68 bitop3:0x36
	v_bitop3_b32 v55, v3, v11, s68 bitop3:0x36
	v_bitop3_b32 v54, v2, v10, s68 bitop3:0x36
	v_ashrrev_i32_e32 v2, 31, v14
	v_ashrrev_i32_e32 v3, 31, v15
	v_ashrrev_i32_e32 v4, 31, v16
	v_ashrrev_i32_e32 v5, 31, v17
	s_cselect_b64 s[40:41], -1, 0
	s_cmp_le_u32 s26, s44
	v_add_u32_e32 v65, s28, v142
	v_bitop3_b32 v61, v5, v17, s68 bitop3:0x36
	v_bitop3_b32 v60, v4, v16, s68 bitop3:0x36
	v_bitop3_b32 v59, v3, v15, s68 bitop3:0x36
	v_bitop3_b32 v58, v2, v14, s68 bitop3:0x36
	v_readlane_b32 s29, v253, 5
	s_cbranch_scc1 .LBB0_651
	v_or_b32_e32 v2, 2, v65
	v_cmp_le_i32_e32 vcc, v65, v124
	v_add_u32_e32 v5, 11, v65
	v_add_u32_e32 v4, 10, v65
	v_cndmask_b32_e32 v105, 0, v105, vcc
	v_cmp_le_i32_e32 vcc, v2, v124
	v_or_b32_e32 v2, 3, v65
	v_add_u32_e32 v3, 9, v65
	v_cndmask_b32_e32 v104, 0, v104, vcc
	v_cmp_lt_i32_e32 vcc, v65, v124
	s_nop 1
	v_cndmask_b32_e32 v106, 0, v106, vcc
	v_cmp_ge_i32_e32 vcc, v124, v2
	v_add_u32_e32 v2, 8, v65
	s_nop 0
	v_cndmask_b32_e32 v107, 0, v107, vcc
	v_cmp_le_i32_e32 vcc, v5, v124
	v_add_u32_e32 v5, 19, v65
	s_nop 0
	v_cndmask_b32_e32 v69, 0, v69, vcc
	v_cmp_le_i32_e32 vcc, v4, v124
	v_add_u32_e32 v4, 18, v65
	s_nop 0
	v_cndmask_b32_e32 v68, 0, v68, vcc
	v_cmp_le_i32_e32 vcc, v3, v124
	v_add_u32_e32 v3, 17, v65
	s_nop 0
	v_cndmask_b32_e32 v67, 0, v67, vcc
	v_cmp_le_i32_e32 vcc, v2, v124
	v_add_u32_e32 v2, 16, v65
	s_nop 0
	v_cndmask_b32_e32 v66, 0, v66, vcc
	v_cmp_le_i32_e32 vcc, v5, v124
	v_add_u32_e32 v5, 27, v65
	s_nop 0
	v_cndmask_b32_e32 v57, 0, v57, vcc
	v_cmp_le_i32_e32 vcc, v4, v124
	v_add_u32_e32 v4, 26, v65
	s_nop 0
	v_cndmask_b32_e32 v56, 0, v56, vcc
	v_cmp_le_i32_e32 vcc, v3, v124
	v_add_u32_e32 v3, 25, v65
	s_nop 0
	v_cndmask_b32_e32 v55, 0, v55, vcc
	v_cmp_le_i32_e32 vcc, v2, v124
	v_add_u32_e32 v2, 24, v65
	s_nop 0
	v_cndmask_b32_e32 v54, 0, v54, vcc
	v_cmp_le_i32_e32 vcc, v5, v124
	s_nop 1
	v_cndmask_b32_e32 v61, 0, v61, vcc
	v_cmp_le_i32_e32 vcc, v4, v124
	s_nop 1
	v_cndmask_b32_e32 v60, 0, v60, vcc
	v_cmp_le_i32_e32 vcc, v3, v124
	s_nop 1
	v_cndmask_b32_e32 v59, 0, v59, vcc
	v_cmp_le_i32_e32 vcc, v2, v124
	s_nop 1
	v_cndmask_b32_e32 v58, 0, v58, vcc

; __device__ __forceinline__ unsigned ordkey(float f) { const unsigned u = __float_as_uint(f); return u ^ ((unsigned)((int)u >> 31) | 0x80000000u); }
; __device__ __forceinline__ int crow(int r, int hi) { return (r & 3) + 8 * (r >> 2) + 4 * hi; }
; __global__ void __launch_bounds__(NWAVES * 64, 2) mega_fwd(Args args) {
;     ...
;                         for (int h = 0; h < 8; ++h) { fa::f32x16 a;
; #pragma unroll
;                             for (int r = 0; r < 16; ++r) a[r] = 0.f;
;                             a = __builtin_amdgcn_mfma_f32_32x32x16_f16(kf0, __builtin_bit_cast(f16x8, iqL[(2 * h) * 64 + lane]), a, 0, 0, 0);
;                             a = __builtin_amdgcn_mfma_f32_32x32x16_f16(kf1, __builtin_bit_cast(f16x8, iqL[(2 * h + 1) * 64 + lane]), a, 0, 0, 0);
;                             const float sg = ((sgnbits >> h) & 1u) ? -1.f : 1.f;
; #pragma unroll
;                             for (int r = 0; r < 16; ++r) sc[r] = __builtin_fmaf(__builtin_fabsf(a[r]), sg, sc[r]); }
; #pragma unroll
;                         for (int r = 0; r < 16; ++r) keys[ti][16 * half + r] = ordkey(sc[r]);
;                         if (k0 + 63 > 32 * qg) {
; #pragma unroll
;                             for (int r = 0; r < 16; ++r) { const int kidx = k0 + 32 * half + fa::crow(r, hi); keys[ti][16 * half + r] = (kidx <= t) ? keys[ti][16 * half + r] : 0u; } } }
.LBB0_652:
	ds_read_b128 v[18:21], v141
	ds_read_b128 v[70:73], v141 offset:1024
	ds_read_b128 v[224:227], v141 offset:2048
	ds_read_b128 v[176:179], v141 offset:3072
	s_waitcnt lgkmcnt(3)
	v_mfma_f32_32x32x16_f16 v[18:33], v[38:41], v[18:21], 0
	s_waitcnt lgkmcnt(2)
	v_mfma_f32_32x32x16_f16 v[18:33], v[34:37], v[70:73], v[18:33]
	s_waitcnt lgkmcnt(1)
	v_mfma_f32_32x32x16_f16 v[208:223], v[38:41], v[224:227], 0
	s_waitcnt lgkmcnt(0)
	v_mfma_f32_32x32x16_f16 v[208:223], v[34:37], v[176:179], v[208:223]
	v_bfe_u32 v70, v140, s26, 1
	v_cmp_eq_u32_e32 vcc, 0, v70
	v_lshrrev_b32_e32 v180, s26, v140
	v_and_b32_e32 v180, 2, v180
	v_cndmask_b32_e64 v70, -1.0, 1.0, vcc
	v_cmp_eq_u32_e32 vcc, 0, v180
	v_add_u32_e32 v141, 0x1000, v141
	s_add_i32 s26, s26, 2
	v_cndmask_b32_e64 v180, -1.0, 1.0, vcc
	s_cmp_lg_u32 s26, 8
	v_fma_f32 v72, |v18|, v70, v2
	v_fma_f32 v73, |v19|, v70, v3
	v_fma_f32 v100, |v20|, v70, v4
	v_fma_f32 v101, |v21|, v70, v5
	v_fma_f32 v22, |v22|, v70, v6
	v_fma_f32 v23, |v23|, v70, v7
	v_fma_f32 v24, |v24|, v70, v8
	v_fma_f32 v25, |v25|, v70, v9
	v_fma_f32 v26, |v26|, v70, v10
	v_fma_f32 v27, |v27|, v70, v11
	v_fma_f32 v28, |v28|, v70, v12
	v_fma_f32 v29, |v29|, v70, v13
	v_fma_f32 v30, |v30|, v70, v14
	v_fma_f32 v31, |v31|, v70, v15
	v_fma_f32 v32, |v32|, v70, v16
	v_fma_f32 v33, |v33|, v70, v17
	v_fma_f32 v4, |v210|, v180, v100
	v_fma_f32 v5, |v211|, v180, v101
	v_fma_f32 v2, |v208|, v180, v72
	v_fma_f32 v3, |v209|, v180, v73
	v_fma_f32 v8, |v214|, v180, v24
	v_fma_f32 v9, |v215|, v180, v25
	v_fma_f32 v6, |v212|, v180, v22
	v_fma_f32 v7, |v213|, v180, v23
	v_fma_f32 v12, |v218|, v180, v28
	v_fma_f32 v13, |v219|, v180, v29
	v_fma_f32 v10, |v216|, v180, v26
	v_fma_f32 v11, |v217|, v180, v27
	v_fma_f32 v16, |v222|, v180, v32
	v_fma_f32 v17, |v223|, v180, v33
	v_fma_f32 v14, |v220|, v180, v30
	v_fma_f32 v15, |v221|, v180, v31
	s_cbranch_scc1 .LBB0_652
	v_ashrrev_i32_e32 v18, 31, v2
	v_ashrrev_i32_e32 v19, 31, v3
	v_ashrrev_i32_e32 v20, 31, v4
	v_ashrrev_i32_e32 v21, 31, v5
	v_bitop3_b32 v21, v21, v5, s68 bitop3:0x36
	v_bitop3_b32 v25, v20, v4, s68 bitop3:0x36
	v_bitop3_b32 v23, v19, v3, s68 bitop3:0x36
	v_bitop3_b32 v26, v18, v2, s68 bitop3:0x36
	v_ashrrev_i32_e32 v2, 31, v6
	v_ashrrev_i32_e32 v3, 31, v7
	v_ashrrev_i32_e32 v4, 31, v8
	v_ashrrev_i32_e32 v5, 31, v9
	v_bitop3_b32 v18, v5, v9, s68 bitop3:0x36
	v_bitop3_b32 v20, v4, v8, s68 bitop3:0x36
	v_bitop3_b32 v24, v3, v7, s68 bitop3:0x36
	v_bitop3_b32 v22, v2, v6, s68 bitop3:0x36
	v_ashrrev_i32_e32 v2, 31, v10
	v_ashrrev_i32_e32 v3, 31, v11
	v_ashrrev_i32_e32 v4, 31, v12
	v_ashrrev_i32_e32 v5, 31, v13
	v_bitop3_b32 v13, v5, v13, s68 bitop3:0x36
	v_bitop3_b32 v9, v4, v12, s68 bitop3:0x36
	v_bitop3_b32 v11, v3, v11, s68 bitop3:0x36
	v_bitop3_b32 v19, v2, v10, s68 bitop3:0x36
	v_ashrrev_i32_e32 v3, 31, v14
	v_ashrrev_i32_e32 v4, 31, v15
	v_ashrrev_i32_e32 v5, 31, v16
	v_ashrrev_i32_e32 v2, 31, v17
	v_bitop3_b32 v2, v2, v17, s68 bitop3:0x36
	v_bitop3_b32 v8, v5, v16, s68 bitop3:0x36
	v_bitop3_b32 v10, v4, v15, s68 bitop3:0x36
	s_andn2_b64 vcc, exec, s[40:41]
	v_bitop3_b32 v12, v3, v14, s68 bitop3:0x36
	s_cbranch_vccnz .LBB0_659
	v_add_u32_e32 v3, 32, v65
	v_or_b32_e32 v5, 2, v3
	v_or_b32_e32 v4, 3, v3
	v_cmp_le_i32_e32 vcc, v5, v124
	v_add_u32_e32 v6, 40, v65
	v_add_u32_e32 v5, 41, v65
	v_cndmask_b32_e32 v25, 0, v25, vcc
	v_cmp_le_i32_e32 vcc, v4, v124
	v_add_u32_e32 v4, 42, v65
	s_nop 0
	v_cndmask_b32_e32 v21, 0, v21, vcc
	v_cmp_le_i32_e32 vcc, v3, v124
	s_nop 1
	v_cndmask_b32_e32 v26, 0, v26, vcc
	v_cmp_gt_i32_e32 vcc, v124, v3
	v_add_u32_e32 v3, 43, v65
	s_nop 0
	v_cndmask_b32_e32 v23, 0, v23, vcc
	v_cmp_le_i32_e32 vcc, v6, v124
	v_add_u32_e32 v6, 48, v65
	s_nop 0
	v_cndmask_b32_e32 v22, 0, v22, vcc
	v_cmp_le_i32_e32 vcc, v5, v124
	v_add_u32_e32 v5, 49, v65
	s_nop 0
	v_cndmask_b32_e32 v24, 0, v24, vcc
	v_cmp_le_i32_e32 vcc, v4, v124
	v_add_u32_e32 v4, 50, v65
	s_nop 0
	v_cndmask_b32_e32 v20, 0, v20, vcc
	v_cmp_le_i32_e32 vcc, v3, v124
	v_add_u32_e32 v3, 51, v65
	s_nop 0
	v_cndmask_b32_e32 v18, 0, v18, vcc
	v_cmp_le_i32_e32 vcc, v6, v124
	v_add_u32_e32 v6, 56, v65
	s_nop 0
	v_cndmask_b32_e32 v19, 0, v19, vcc
	v_cmp_le_i32_e32 vcc, v5, v124
	v_add_u32_e32 v5, 57, v65
	s_nop 0
	v_cndmask_b32_e32 v11, 0, v11, vcc
	v_cmp_le_i32_e32 vcc, v4, v124
	v_add_u32_e32 v4, 58, v65
	s_nop 0
	v_cndmask_b32_e32 v9, 0, v9, vcc
	v_cmp_le_i32_e32 vcc, v3, v124
	v_add_u32_e32 v3, 59, v65
	s_nop 0
	v_cndmask_b32_e32 v13, 0, v13, vcc
	v_cmp_le_i32_e32 vcc, v6, v124
	s_nop 1
	v_cndmask_b32_e32 v12, 0, v12, vcc
	v_cmp_le_i32_e32 vcc, v5, v124
	s_nop 1
	v_cndmask_b32_e32 v10, 0, v10, vcc
	v_cmp_le_i32_e32 vcc, v4, v124
	s_nop 1
	v_cndmask_b32_e32 v8, 0, v8, vcc
	v_cmp_le_i32_e32 vcc, v3, v124
	s_nop 1
	v_cndmask_b32_e32 v2, 0, v2, vcc
	s_branch .LBB0_659
